# in-projection GEMM K loop: loop-top full vmcnt drain relaxed to the schedule's vmcnt(6) (on top of v11)
# speedup vs baseline: 1.0417x; 1.0085x over previous
.LBB0_301:
	s_waitcnt vmcnt(6)
	ds_read_b128 v[106:109], v213
	ds_read_b128 v[110:113], v213 offset:1024
	ds_read_b128 v[126:129], v213 offset:2048
	ds_read_b128 v[130:133], v213 offset:3072
	s_add_u32 s68, s66, 0xfff80080
	s_addc_u32 s69, s67, -1
	s_cmp_eq_u32 s94, 28
	s_cselect_b32 s71, s11, s69
	s_cselect_b32 s70, s16, s68
	s_cselect_b32 s69, s57, s93
	s_cselect_b32 s68, s59, s92
	v_lshl_add_u64 v[202:203], s[66:67], 0, v[170:171]
	s_add_i32 m0, s65, 0xc000
	ds_read_b128 v[146:149], v214
	ds_read_b128 v[178:181], v214 offset:1024
	ds_read_b128 v[182:185], v214 offset:2048
	ds_read_b128 v[186:189], v214 offset:3072
	ds_read_b128 v[190:193], v214 offset:4096
	ds_read_b128 v[194:197], v214 offset:5120
	ds_read_b128 v[198:201], v214 offset:6144
	ds_read_b128 v[220:223], v214 offset:7168
	global_load_lds_dwordx4 v[202:203], off
	v_lshl_add_u64 v[202:203], s[66:67], 0, v[172:173]
	s_add_i32 m0, s65, 0xe000
	s_nop 0
	global_load_lds_dwordx4 v[202:203], off
	s_waitcnt lgkmcnt(8)
	s_barrier
	s_waitcnt lgkmcnt(0)
	s_setprio 1
	s_waitcnt lgkmcnt(0)
	v_mfma_i32_16x16x64_i8 v[142:145], v[106:109], v[146:149], v[142:145]
	v_mfma_i32_16x16x64_i8 v[138:141], v[126:129], v[146:149], v[138:141]
	v_mfma_i32_16x16x64_i8 v[118:121], v[106:109], v[182:185], v[118:121]
	v_mfma_i32_16x16x64_i8 v[114:117], v[126:129], v[182:185], v[114:117]
	v_mfma_i32_16x16x64_i8 v[94:97], v[106:109], v[190:193], v[94:97]
	v_mfma_i32_16x16x64_i8 v[90:93], v[126:129], v[190:193], v[90:93]
	v_mfma_i32_16x16x64_i8 v[78:81], v[106:109], v[198:201], v[78:81]
	v_mfma_i32_16x16x64_i8 v[74:77], v[126:129], v[198:201], v[74:77]
	v_mfma_i32_16x16x64_i8 v[142:145], v[110:113], v[178:181], v[142:145]
	v_mfma_i32_16x16x64_i8 v[138:141], v[130:133], v[178:181], v[138:141]
	v_mfma_i32_16x16x64_i8 v[118:121], v[110:113], v[186:189], v[118:121]
	v_mfma_i32_16x16x64_i8 v[114:117], v[130:133], v[186:189], v[114:117]
	v_mfma_i32_16x16x64_i8 v[94:97], v[110:113], v[194:197], v[94:97]
	v_mfma_i32_16x16x64_i8 v[90:93], v[130:133], v[194:197], v[90:93]
	v_mfma_i32_16x16x64_i8 v[78:81], v[110:113], v[220:223], v[78:81]
	v_mfma_i32_16x16x64_i8 v[74:77], v[130:133], v[220:223], v[74:77]
	s_setprio 0
	s_barrier
	s_add_i32 s95, s89, s75
	v_lshl_add_u64 v[202:203], s[68:69], 0, v[152:153]
	s_mov_b32 m0, s95
	ds_read_b128 v[224:227], v215
	ds_read_b128 v[228:231], v215 offset:1024
	ds_read_b128 v[232:235], v215 offset:2048
	ds_read_b128 v[236:239], v215 offset:3072
	global_load_lds_dwordx4 v[202:203], off
	v_lshl_add_u64 v[240:241], s[68:69], 0, v[156:157]
	s_add_i32 m0, s95, 0x2000
	s_nop 0
	global_load_lds_dwordx4 v[240:241], off
	s_barrier
	s_waitcnt lgkmcnt(0)
	s_setprio 1
	s_waitcnt lgkmcnt(0)
	v_mfma_i32_16x16x64_i8 v[134:137], v[224:227], v[146:149], v[134:137]
	v_mfma_i32_16x16x64_i8 v[122:125], v[232:235], v[146:149], v[122:125]
	v_mfma_i32_16x16x64_i8 v[102:105], v[224:227], v[182:185], v[102:105]
	v_mfma_i32_16x16x64_i8 v[98:101], v[232:235], v[182:185], v[98:101]
	v_mfma_i32_16x16x64_i8 v[86:89], v[224:227], v[190:193], v[86:89]
	v_mfma_i32_16x16x64_i8 v[82:85], v[232:235], v[190:193], v[82:85]
	v_mfma_i32_16x16x64_i8 v[70:73], v[224:227], v[198:201], v[70:73]
	v_mfma_i32_16x16x64_i8 v[66:69], v[232:235], v[198:201], v[66:69]
	v_mfma_i32_16x16x64_i8 v[134:137], v[228:231], v[178:181], v[134:137]
	v_mfma_i32_16x16x64_i8 v[122:125], v[236:239], v[178:181], v[122:125]
	v_mfma_i32_16x16x64_i8 v[102:105], v[228:231], v[186:189], v[102:105]
	v_mfma_i32_16x16x64_i8 v[98:101], v[236:239], v[186:189], v[98:101]
	v_mfma_i32_16x16x64_i8 v[86:89], v[228:231], v[194:197], v[86:89]
	v_mfma_i32_16x16x64_i8 v[82:85], v[236:239], v[194:197], v[82:85]
	v_mfma_i32_16x16x64_i8 v[70:73], v[228:231], v[220:223], v[70:73]
	v_mfma_i32_16x16x64_i8 v[66:69], v[236:239], v[220:223], v[66:69]
	s_setprio 0
	s_mov_b32 m0, s65
	v_lshl_add_u64 v[242:243], s[70:71], 0, v[150:151]
	s_barrier
	ds_read_b128 v[146:149], v214 offset:16384
	ds_read_b128 v[178:181], v214 offset:17408
	ds_read_b128 v[182:185], v214 offset:18432
	ds_read_b128 v[186:189], v214 offset:19456
	ds_read_b128 v[190:193], v214 offset:20480
	ds_read_b128 v[194:197], v214 offset:21504
	ds_read_b128 v[198:201], v214 offset:22528
	ds_read_b128 v[220:223], v214 offset:23552
	global_load_lds_dwordx4 v[242:243], off
	v_lshl_add_u64 v[244:245], s[70:71], 0, v[154:155]
	s_mov_b32 m0, s76
	s_nop 0
	global_load_lds_dwordx4 v[244:245], off
	s_barrier
	s_waitcnt lgkmcnt(0)
	s_setprio 1
	s_waitcnt lgkmcnt(0)
	v_mfma_i32_16x16x64_i8 v[62:65], v[106:109], v[146:149], v[62:65]
	v_mfma_i32_16x16x64_i8 v[58:61], v[126:129], v[146:149], v[58:61]
	v_mfma_i32_16x16x64_i8 v[46:49], v[106:109], v[182:185], v[46:49]
	v_mfma_i32_16x16x64_i8 v[42:45], v[126:129], v[182:185], v[42:45]
	v_mfma_i32_16x16x64_i8 v[30:33], v[106:109], v[190:193], v[30:33]
	v_mfma_i32_16x16x64_i8 v[26:29], v[126:129], v[190:193], v[26:29]
	v_mfma_i32_16x16x64_i8 v[14:17], v[106:109], v[198:201], v[14:17]
	v_mfma_i32_16x16x64_i8 v[10:13], v[126:129], v[198:201], v[10:13]
	v_mfma_i32_16x16x64_i8 v[62:65], v[110:113], v[178:181], v[62:65]
	v_mfma_i32_16x16x64_i8 v[58:61], v[130:133], v[178:181], v[58:61]
	v_mfma_i32_16x16x64_i8 v[46:49], v[110:113], v[186:189], v[46:49]
	v_mfma_i32_16x16x64_i8 v[42:45], v[130:133], v[186:189], v[42:45]
	v_mfma_i32_16x16x64_i8 v[30:33], v[110:113], v[194:197], v[30:33]
	v_mfma_i32_16x16x64_i8 v[26:29], v[130:133], v[194:197], v[26:29]
	v_mfma_i32_16x16x64_i8 v[14:17], v[110:113], v[220:223], v[14:17]
	v_mfma_i32_16x16x64_i8 v[10:13], v[130:133], v[220:223], v[10:13]
	s_setprio 0
	s_barrier
	s_add_u32 s96, s68, 0x80000
	s_addc_u32 s97, s69, 0
	s_add_i32 s95, s90, s75
	v_lshl_add_u64 v[106:107], s[96:97], 0, v[152:153]
	s_mov_b32 m0, s95
	s_nop 0
	global_load_lds_dwordx4 v[106:107], off
	v_lshl_add_u64 v[106:107], s[96:97], 0, v[156:157]
	s_add_i32 m0, s95, 0x2000
	s_nop 0
	global_load_lds_dwordx4 v[106:107], off
	s_waitcnt vmcnt(6)
	s_barrier
	s_setprio 1
	v_mfma_i32_16x16x64_i8 v[54:57], v[224:227], v[146:149], v[54:57]
	v_mfma_i32_16x16x64_i8 v[50:53], v[232:235], v[146:149], v[50:53]
	v_mfma_i32_16x16x64_i8 v[38:41], v[224:227], v[182:185], v[38:41]
	v_mfma_i32_16x16x64_i8 v[34:37], v[232:235], v[182:185], v[34:37]
	v_mfma_i32_16x16x64_i8 v[22:25], v[224:227], v[190:193], v[22:25]
	v_mfma_i32_16x16x64_i8 v[18:21], v[232:235], v[190:193], v[18:21]
	v_mfma_i32_16x16x64_i8 v[6:9], v[224:227], v[198:201], v[6:9]
	v_mfma_i32_16x16x64_i8 v[2:5], v[232:235], v[198:201], v[2:5]
	v_mfma_i32_16x16x64_i8 v[54:57], v[228:231], v[178:181], v[54:57]
	v_mfma_i32_16x16x64_i8 v[50:53], v[236:239], v[178:181], v[50:53]
	v_mfma_i32_16x16x64_i8 v[38:41], v[228:231], v[186:189], v[38:41]
	v_mfma_i32_16x16x64_i8 v[34:37], v[236:239], v[186:189], v[34:37]
	v_mfma_i32_16x16x64_i8 v[22:25], v[228:231], v[194:197], v[22:25]
	v_mfma_i32_16x16x64_i8 v[18:21], v[236:239], v[194:197], v[18:21]
	v_mfma_i32_16x16x64_i8 v[6:9], v[228:231], v[220:223], v[6:9]
	v_mfma_i32_16x16x64_i8 v[2:5], v[236:239], v[220:223], v[2:5]
	s_setprio 0
	s_add_i32 s95, 0, 0x18000
	v_add_u32_e32 v130, s95, v163
	s_barrier
	ds_read_b128 v[106:109], v130
	ds_read_b128 v[110:113], v130 offset:1024
	ds_read_b128 v[126:129], v130 offset:2048
	ds_read_b128 v[130:133], v130 offset:3072
	s_add_u32 s70, s70, 0x80000
	s_addc_u32 s71, s71, 0
	s_mov_b32 m0, s77
	v_lshl_add_u64 v[224:225], s[70:71], 0, v[150:151]
	ds_read_b128 v[146:149], v214 offset:32768
	ds_read_b128 v[178:181], v214 offset:33792
	ds_read_b128 v[182:185], v214 offset:34816
	ds_read_b128 v[186:189], v214 offset:35840
	ds_read_b128 v[190:193], v214 offset:36864
	ds_read_b128 v[194:197], v214 offset:37888
	ds_read_b128 v[198:201], v214 offset:38912
	ds_read_b128 v[220:223], v214 offset:39936
	global_load_lds_dwordx4 v[224:225], off
	v_lshl_add_u64 v[224:225], s[70:71], 0, v[154:155]
	s_mov_b32 m0, s78
	s_nop 0
	global_load_lds_dwordx4 v[224:225], off
	s_waitcnt lgkmcnt(8)
	s_barrier
	s_waitcnt lgkmcnt(0)
	s_setprio 1
	s_waitcnt lgkmcnt(0)
	v_mfma_i32_16x16x64_i8 v[142:145], v[106:109], v[146:149], v[142:145]
	v_mfma_i32_16x16x64_i8 v[138:141], v[126:129], v[146:149], v[138:141]
	v_mfma_i32_16x16x64_i8 v[118:121], v[106:109], v[182:185], v[118:121]
	v_mfma_i32_16x16x64_i8 v[114:117], v[126:129], v[182:185], v[114:117]
	v_mfma_i32_16x16x64_i8 v[94:97], v[106:109], v[190:193], v[94:97]
	v_mfma_i32_16x16x64_i8 v[90:93], v[126:129], v[190:193], v[90:93]
	v_mfma_i32_16x16x64_i8 v[78:81], v[106:109], v[198:201], v[78:81]
	v_mfma_i32_16x16x64_i8 v[74:77], v[126:129], v[198:201], v[74:77]
	v_mfma_i32_16x16x64_i8 v[142:145], v[110:113], v[178:181], v[142:145]
	v_mfma_i32_16x16x64_i8 v[138:141], v[130:133], v[178:181], v[138:141]
	v_mfma_i32_16x16x64_i8 v[118:121], v[110:113], v[186:189], v[118:121]
	v_mfma_i32_16x16x64_i8 v[114:117], v[130:133], v[186:189], v[114:117]
	v_mfma_i32_16x16x64_i8 v[94:97], v[110:113], v[194:197], v[94:97]
	v_mfma_i32_16x16x64_i8 v[90:93], v[130:133], v[194:197], v[90:93]
	v_mfma_i32_16x16x64_i8 v[78:81], v[110:113], v[220:223], v[78:81]
	v_mfma_i32_16x16x64_i8 v[74:77], v[130:133], v[220:223], v[74:77]
	s_setprio 0
	s_barrier
	s_add_i32 s70, 0, 0x1c000
	s_add_i32 s71, s95, s75
	v_add_u32_e32 v158, s70, v163
	v_lshl_add_u64 v[202:203], v[202:203], 0, s[34:35]
	s_mov_b32 m0, s71
	ds_read_b128 v[224:227], v158
	ds_read_b128 v[228:231], v158 offset:1024
	ds_read_b128 v[232:235], v158 offset:2048
	ds_read_b128 v[236:239], v158 offset:3072
	global_load_lds_dwordx4 v[202:203], off
	v_lshl_add_u64 v[202:203], v[240:241], 0, s[34:35]
	s_add_i32 m0, s71, 0x2000
	s_nop 0
	global_load_lds_dwordx4 v[202:203], off
	s_barrier
	s_waitcnt lgkmcnt(0)
	s_setprio 1
	s_waitcnt lgkmcnt(0)
	v_mfma_i32_16x16x64_i8 v[134:137], v[224:227], v[146:149], v[134:137]
	v_mfma_i32_16x16x64_i8 v[122:125], v[232:235], v[146:149], v[122:125]
	v_mfma_i32_16x16x64_i8 v[102:105], v[224:227], v[182:185], v[102:105]
	v_mfma_i32_16x16x64_i8 v[98:101], v[232:235], v[182:185], v[98:101]
	v_mfma_i32_16x16x64_i8 v[86:89], v[224:227], v[190:193], v[86:89]
	v_mfma_i32_16x16x64_i8 v[82:85], v[232:235], v[190:193], v[82:85]
	v_mfma_i32_16x16x64_i8 v[70:73], v[224:227], v[198:201], v[70:73]
	v_mfma_i32_16x16x64_i8 v[66:69], v[232:235], v[198:201], v[66:69]
	v_mfma_i32_16x16x64_i8 v[134:137], v[228:231], v[178:181], v[134:137]
	v_mfma_i32_16x16x64_i8 v[122:125], v[236:239], v[178:181], v[122:125]
	v_mfma_i32_16x16x64_i8 v[102:105], v[228:231], v[186:189], v[102:105]
	v_mfma_i32_16x16x64_i8 v[98:101], v[236:239], v[186:189], v[98:101]
	v_mfma_i32_16x16x64_i8 v[86:89], v[228:231], v[194:197], v[86:89]
	v_mfma_i32_16x16x64_i8 v[82:85], v[236:239], v[194:197], v[82:85]
	v_mfma_i32_16x16x64_i8 v[70:73], v[228:231], v[220:223], v[70:73]
	v_mfma_i32_16x16x64_i8 v[66:69], v[236:239], v[220:223], v[66:69]
	s_setprio 0
	s_mov_b32 m0, s85
	v_lshl_add_u64 v[202:203], v[242:243], 0, s[34:35]
	s_barrier
	ds_read_b128 v[146:149], v214 offset:49152
	ds_read_b128 v[178:181], v214 offset:50176
	ds_read_b128 v[182:185], v214 offset:51200
	ds_read_b128 v[186:189], v214 offset:52224
	ds_read_b128 v[190:193], v214 offset:53248
	ds_read_b128 v[194:197], v214 offset:54272
	ds_read_b128 v[198:201], v214 offset:55296
	ds_read_b128 v[220:223], v214 offset:56320
	global_load_lds_dwordx4 v[202:203], off
	v_lshl_add_u64 v[202:203], v[244:245], 0, s[34:35]
	s_mov_b32 m0, s86
	s_nop 0
	global_load_lds_dwordx4 v[202:203], off
	s_barrier
	s_waitcnt lgkmcnt(0)
	s_setprio 1
	s_waitcnt lgkmcnt(0)
	v_mfma_i32_16x16x64_i8 v[62:65], v[106:109], v[146:149], v[62:65]
	v_mfma_i32_16x16x64_i8 v[58:61], v[126:129], v[146:149], v[58:61]
	v_mfma_i32_16x16x64_i8 v[46:49], v[106:109], v[182:185], v[46:49]
	v_mfma_i32_16x16x64_i8 v[42:45], v[126:129], v[182:185], v[42:45]
	v_mfma_i32_16x16x64_i8 v[30:33], v[106:109], v[190:193], v[30:33]
	v_mfma_i32_16x16x64_i8 v[26:29], v[126:129], v[190:193], v[26:29]
	v_mfma_i32_16x16x64_i8 v[14:17], v[106:109], v[198:201], v[14:17]
	v_mfma_i32_16x16x64_i8 v[10:13], v[126:129], v[198:201], v[10:13]
	v_mfma_i32_16x16x64_i8 v[62:65], v[110:113], v[178:181], v[62:65]
	v_mfma_i32_16x16x64_i8 v[58:61], v[130:133], v[178:181], v[58:61]
	v_mfma_i32_16x16x64_i8 v[46:49], v[110:113], v[186:189], v[46:49]
	v_mfma_i32_16x16x64_i8 v[42:45], v[130:133], v[186:189], v[42:45]
	v_mfma_i32_16x16x64_i8 v[30:33], v[110:113], v[194:197], v[30:33]
	v_mfma_i32_16x16x64_i8 v[26:29], v[130:133], v[194:197], v[26:29]
	v_mfma_i32_16x16x64_i8 v[14:17], v[110:113], v[220:223], v[14:17]
	v_mfma_i32_16x16x64_i8 v[10:13], v[130:133], v[220:223], v[10:13]
	s_setprio 0
	s_barrier
	s_add_u32 s68, s68, 0x80080
	s_addc_u32 s69, s69, 0
	s_add_i32 s70, s70, s75
	v_lshl_add_u64 v[106:107], s[68:69], 0, v[152:153]
	s_mov_b32 m0, s70
	s_nop 0
	global_load_lds_dwordx4 v[106:107], off
	v_lshl_add_u64 v[106:107], s[68:69], 0, v[156:157]
	s_add_i32 m0, s70, 0x2000
	s_nop 0
	global_load_lds_dwordx4 v[106:107], off
	s_waitcnt vmcnt(6)
	s_barrier
	s_setprio 1
	v_mfma_i32_16x16x64_i8 v[54:57], v[224:227], v[146:149], v[54:57]
	v_mfma_i32_16x16x64_i8 v[50:53], v[232:235], v[146:149], v[50:53]
	v_mfma_i32_16x16x64_i8 v[38:41], v[224:227], v[182:185], v[38:41]
	v_mfma_i32_16x16x64_i8 v[34:37], v[232:235], v[182:185], v[34:37]
	v_mfma_i32_16x16x64_i8 v[22:25], v[224:227], v[190:193], v[22:25]
	v_mfma_i32_16x16x64_i8 v[18:21], v[232:235], v[190:193], v[18:21]
	v_mfma_i32_16x16x64_i8 v[6:9], v[224:227], v[198:201], v[6:9]
	v_mfma_i32_16x16x64_i8 v[2:5], v[232:235], v[198:201], v[2:5]
	v_mfma_i32_16x16x64_i8 v[54:57], v[228:231], v[178:181], v[54:57]
	v_mfma_i32_16x16x64_i8 v[50:53], v[236:239], v[178:181], v[50:53]
	v_mfma_i32_16x16x64_i8 v[38:41], v[228:231], v[186:189], v[38:41]
	v_mfma_i32_16x16x64_i8 v[34:37], v[236:239], v[186:189], v[34:37]
	v_mfma_i32_16x16x64_i8 v[22:25], v[228:231], v[194:197], v[22:25]
	v_mfma_i32_16x16x64_i8 v[18:21], v[236:239], v[194:197], v[18:21]
	v_mfma_i32_16x16x64_i8 v[6:9], v[228:231], v[220:223], v[6:9]
	v_mfma_i32_16x16x64_i8 v[2:5], v[236:239], v[220:223], v[2:5]
	s_setprio 0
	s_add_i32 s94, s94, 2
	s_add_u32 s66, s66, 0x100
	s_addc_u32 s67, s67, 0
	s_add_u32 s92, s92, 0x100
	s_addc_u32 s93, s93, 0
	s_cmp_gt_u32 s94, 29
	s_barrier
	s_cbranch_scc0 .LBB0_301
	s_and_b64 vcc, exec, s[36:37]
	s_cbranch_vccz .LBB0_304
	s_barrier
